# baseline (speedup 1.0000x reference)
_Z9ssim_mainPKfS0_S0_Pf:
	s_load_dwordx8 s[4:11], s[0:1], 0x0
	v_readfirstlane_b32 s29, v0
	s_mov_b32 s51, 0x44800000
	s_mov_b32 s38, 0
	s_mov_b32 s39, -1
	s_lshr_b32 s12, s29, 6
	s_and_b32 s13, s2, 7
	s_lshl_b32 s13, s13, 5
	s_lshr_b32 s14, s2, 3
	s_add_u32 s13, s13, s14
	s_lshr_b32 s14, s13, 3
	s_and_b32 s15, s13, 7
	s_lshl_b32 s16, s14, 20
	s_lshl_b32 s17, s15, 17
	s_add_u32 s16, s16, s17
	s_lshl_b32 s17, s12, 8
	s_add_u32 s16, s16, s17
	s_lshl_b32 s27, s12, 2
	s_add_u32 s27, s27, 0x10000
	v_and_b32_e32 v8, 63, v0
	v_and_b32_e32 v169, 15, v0
	v_bfe_u32 v164, v0, 4, 2
	v_lshrrev_b32_e32 v167, 2, v169
	v_lshlrev_b32_e32 v167, 5, v167
	v_and_b32_e32 v168, 1, v169
	v_lshl_or_b32 v167, v168, 4, v167
	v_bfe_u32 v168, v169, 1, 1
	v_lshl_or_b32 v167, v168, 7, v167
	v_lshl_or_b32 v9, v164, 14, v167
	v_and_b32_e32 v168, 1, v164
	v_lshl_or_b32 v23, v168, 14, v167
	v_lshrrev_b32_e32 v168, 1, v164
	v_lshl_or_b32 v23, v168, 13, v23
	v_add_u32_e32 v237, 0x1000, v9
	v_add_u32_e32 v238, 0x2000, v9
	v_add_u32_e32 v239, 0x3000, v9
	v_add_u32_e32 v240, 0x10000, v9
	v_add_u32_e32 v241, 0x11000, v9
	v_add_u32_e32 v242, 0x12000, v9
	v_add_u32_e32 v243, 0x13000, v9
	s_waitcnt lgkmcnt(0)
	s_load_dwordx8 s[40:47], s[8:9], 0x0
	s_load_dwordx2 s[48:49], s[8:9], 0x20
	s_load_dword s50, s[8:9], 0x28
	s_add_u32 s18, s4, s16
	s_addc_u32 s19, s5, 0
	s_add_u32 s20, s6, s16
	s_addc_u32 s21, s7, 0
	global_load_dwordx4 v[36:39], v9, s[18:19] offset:0 sc1 nt
	global_load_dwordx4 v[40:43], v9, s[18:19] offset:2048 sc1 nt
	global_load_dwordx4 v[68:71], v9, s[20:21] offset:0 sc1 nt
	global_load_dwordx4 v[72:75], v9, s[20:21] offset:2048 sc1 nt
	global_load_dwordx4 v[44:47], v237, s[18:19] offset:0 sc1 nt
	global_load_dwordx4 v[48:51], v237, s[18:19] offset:2048 sc1 nt
	global_load_dwordx4 v[76:79], v237, s[20:21] offset:0 sc1 nt
	global_load_dwordx4 v[80:83], v237, s[20:21] offset:2048 sc1 nt
	global_load_dwordx4 v[52:55], v238, s[18:19] offset:0 sc1 nt
	global_load_dwordx4 v[56:59], v238, s[18:19] offset:2048 sc1 nt
	global_load_dwordx4 v[84:87], v238, s[20:21] offset:0 sc1 nt
	global_load_dwordx4 v[88:91], v238, s[20:21] offset:2048 sc1 nt
	global_load_dwordx4 v[60:63], v239, s[18:19] offset:0 sc1 nt
	global_load_dwordx4 v[64:67], v239, s[18:19] offset:2048 sc1 nt
	global_load_dwordx4 v[92:95], v239, s[20:21] offset:0 sc1 nt
	global_load_dwordx4 v[96:99], v239, s[20:21] offset:2048 sc1 nt
	v_mov_b32_e32 v6, s27
	v_mov_b32_e32 v168, 0
	ds_write_b32 v6, v168 offset:0
	ds_write_b32 v6, v168 offset:32
	ds_write_b32 v6, v168 offset:64
	ds_write_b32 v6, v168 offset:96
	v_lshlrev_b32_e32 v167, 3, v164
	v_xor_b32_e32 v168, 16, v167
	v_sub_u32_e32 v165, v167, v169
	v_sub_u32_e32 v166, v168, v169
	v_add_u32_e32 v172, 0, v165
	v_min_u32_e32 v172, 11, v172
	v_lshlrev_b32_e32 v172, 2, v172
	v_add_u32_e32 v173, 1, v165
	v_min_u32_e32 v173, 11, v173
	v_lshlrev_b32_e32 v173, 2, v173
	v_add_u32_e32 v174, 2, v165
	v_min_u32_e32 v174, 11, v174
	v_lshlrev_b32_e32 v174, 2, v174
	v_add_u32_e32 v175, 3, v165
	v_min_u32_e32 v175, 11, v175
	v_lshlrev_b32_e32 v175, 2, v175
	v_add_u32_e32 v176, 4, v165
	v_min_u32_e32 v176, 11, v176
	v_lshlrev_b32_e32 v176, 2, v176
	v_add_u32_e32 v177, 5, v165
	v_min_u32_e32 v177, 11, v177
	v_lshlrev_b32_e32 v177, 2, v177
	v_add_u32_e32 v178, 6, v165
	v_min_u32_e32 v178, 11, v178
	v_lshlrev_b32_e32 v178, 2, v178
	v_add_u32_e32 v179, 7, v165
	v_min_u32_e32 v179, 11, v179
	v_lshlrev_b32_e32 v179, 2, v179
	v_add_u32_e32 v180, 0, v166
	v_min_u32_e32 v180, 11, v180
	v_lshlrev_b32_e32 v180, 2, v180
	v_add_u32_e32 v181, 1, v166
	v_min_u32_e32 v181, 11, v181
	v_lshlrev_b32_e32 v181, 2, v181
	v_add_u32_e32 v182, 2, v166
	v_min_u32_e32 v182, 11, v182
	v_lshlrev_b32_e32 v182, 2, v182
	v_add_u32_e32 v183, 3, v166
	v_min_u32_e32 v183, 11, v183
	v_lshlrev_b32_e32 v183, 2, v183
	v_add_u32_e32 v184, 4, v166
	v_min_u32_e32 v184, 11, v184
	v_lshlrev_b32_e32 v184, 2, v184
	v_add_u32_e32 v185, 5, v166
	v_min_u32_e32 v185, 11, v185
	v_lshlrev_b32_e32 v185, 2, v185
	v_add_u32_e32 v186, 6, v166
	v_min_u32_e32 v186, 11, v186
	v_lshlrev_b32_e32 v186, 2, v186
	v_add_u32_e32 v187, 7, v166
	v_min_u32_e32 v187, 11, v187
	v_lshlrev_b32_e32 v187, 2, v187
	s_cmp_eq_u32 s15, 7
	s_cselect_b32 s22, 0, 0x20000
	s_add_u32 s84, s18, s22
	s_addc_u32 s85, s19, 0
	s_add_u32 s86, s18, s22
	s_addc_u32 s87, s19, 0
	s_add_u32 s86, s86, 0x1000
	s_addc_u32 s87, s87, 0
	s_add_u32 s88, s20, s22
	s_addc_u32 s89, s21, 0
	s_add_u32 s90, s20, s22
	s_addc_u32 s91, s21, 0
	s_add_u32 s90, s90, 0x1000
	s_addc_u32 s91, s91, 0
	s_waitcnt lgkmcnt(0)
	v_writelane_b32 v171, s40, 0
	v_writelane_b32 v171, s41, 1
	v_writelane_b32 v171, s42, 2
	v_writelane_b32 v171, s43, 3
	v_writelane_b32 v171, s44, 4
	v_writelane_b32 v171, s45, 5
	v_writelane_b32 v171, s46, 6
	v_writelane_b32 v171, s47, 7
	v_writelane_b32 v171, s48, 8
	v_writelane_b32 v171, s49, 9
	v_writelane_b32 v171, s50, 10
	v_writelane_b32 v171, 0, 11
	v_fma_mixlo_f16 v171, v171, s51, 0
	ds_bpermute_b32 v188, v172, v171
	ds_bpermute_b32 v189, v173, v171
	ds_bpermute_b32 v190, v174, v171
	ds_bpermute_b32 v191, v175, v171
	ds_bpermute_b32 v192, v176, v171
	ds_bpermute_b32 v193, v177, v171
	ds_bpermute_b32 v194, v178, v171
	ds_bpermute_b32 v195, v179, v171
	v_mov_b32_e32 v229, 0x44800000
	v_fma_mixlo_f16 v228, s40, v229, 0
	v_cvt_f32_f16_e32 v228, v228
	v_cvt_f64_f32_e32 v[212:213], v228
	v_add_f64 v[212:213], v[212:213], 0
	v_fma_mixlo_f16 v228, s41, v229, 0
	v_cvt_f32_f16_e32 v228, v228
	v_cvt_f64_f32_e32 v[214:215], v228
	v_add_f64 v[212:213], v[212:213], v[214:215]
	v_fma_mixlo_f16 v228, s42, v229, 0
	v_cvt_f32_f16_e32 v228, v228
	v_cvt_f64_f32_e32 v[214:215], v228
	v_add_f64 v[212:213], v[212:213], v[214:215]
	v_fma_mixlo_f16 v228, s43, v229, 0
	v_cvt_f32_f16_e32 v228, v228
	v_cvt_f64_f32_e32 v[214:215], v228
	v_add_f64 v[212:213], v[212:213], v[214:215]
	v_fma_mixlo_f16 v228, s44, v229, 0
	v_cvt_f32_f16_e32 v228, v228
	v_cvt_f64_f32_e32 v[214:215], v228
	v_add_f64 v[212:213], v[212:213], v[214:215]
	v_fma_mixlo_f16 v228, s45, v229, 0
	v_cvt_f32_f16_e32 v228, v228
	v_cvt_f64_f32_e32 v[214:215], v228
	v_add_f64 v[212:213], v[212:213], v[214:215]
	v_fma_mixlo_f16 v228, s46, v229, 0
	v_cvt_f32_f16_e32 v228, v228
	v_cvt_f64_f32_e32 v[214:215], v228
	v_add_f64 v[212:213], v[212:213], v[214:215]
	v_fma_mixlo_f16 v228, s47, v229, 0
	v_cvt_f32_f16_e32 v228, v228
	v_cvt_f64_f32_e32 v[214:215], v228
	v_add_f64 v[212:213], v[212:213], v[214:215]
	v_fma_mixlo_f16 v228, s48, v229, 0
	v_cvt_f32_f16_e32 v228, v228
	v_cvt_f64_f32_e32 v[214:215], v228
	v_add_f64 v[212:213], v[212:213], v[214:215]
	v_fma_mixlo_f16 v228, s49, v229, 0
	v_cvt_f32_f16_e32 v228, v228
	v_cvt_f64_f32_e32 v[214:215], v228
	v_add_f64 v[212:213], v[212:213], v[214:215]
	v_fma_mixlo_f16 v228, s50, v229, 0
	v_cvt_f32_f16_e32 v228, v228
	v_cvt_f64_f32_e32 v[214:215], v228
	v_add_f64 v[212:213], v[212:213], v[214:215]
	s_waitcnt lgkmcnt(7)
	ds_bpermute_b32 v196, v180, v171
	ds_bpermute_b32 v197, v181, v171
	ds_bpermute_b32 v198, v182, v171
	ds_bpermute_b32 v199, v183, v171
	ds_bpermute_b32 v200, v184, v171
	ds_bpermute_b32 v201, v185, v171
	ds_bpermute_b32 v202, v186, v171
	ds_bpermute_b32 v203, v187, v171
	v_mul_f64 v[212:213], v[212:213], v[212:213]
	v_mul_f64 v[216:217], v[212:213], 0.5
	v_add_f64 v[218:219], v[216:217], v[216:217]
	s_mov_b32 s36, 0xeb1c432d
	s_mov_b32 s37, 0x3f1a36e2
	v_mul_f64 v[220:221], v[212:213], s[36:37]
	v_mul_f64 v[222:223], v[216:217], v[218:219]
	v_fmac_f64_e32 v[222:223], v[212:213], v[220:221]
	v_add_f64 v[224:225], v[212:213], v[212:213]
	s_mov_b32 s36, 0x487fcb92
	s_mov_b32 s37, 0x3f4d7dbf
	v_mul_f64 v[226:227], v[212:213], s[36:37]
	v_cvt_f32_f64_e32 v0, v[226:227]
	v_mov_b32_e32 v1, v0
	v_mov_b32_e32 v2, v0
	v_mov_b32_e32 v3, v0
	v_cvt_f32_f64_e32 v10, v[218:219]
	v_cvt_f32_f64_e32 v11, v[222:223]
	v_cvt_f32_f64_e32 v12, v[212:213]
	v_cvt_f32_f64_e32 v13, v[224:225]
	v_mul_f64 v[226:227], v[212:213], v[226:227]
	v_cvt_f32_f64_e32 v14, v[226:227]
	v_lshlrev_b32_e32 v167, 2, v164
	s_cmp_eq_u32 s12, 0
	s_cselect_b32 s23, 6, 64
	v_add_u32_e32 v168, 0, v167
	v_cmp_gt_u32_e32 vcc, s23, v168
	s_nop 1
	v_cndmask_b32_e64 v15, 0, 1.0, vcc
	v_add_u32_e32 v168, 1, v167
	v_cmp_gt_u32_e32 vcc, s23, v168
	s_nop 1
	v_cndmask_b32_e64 v16, 0, 1.0, vcc
	v_add_u32_e32 v168, 2, v167
	v_cmp_gt_u32_e32 vcc, s23, v168
	s_nop 1
	v_cndmask_b32_e64 v17, 0, 1.0, vcc
	v_add_u32_e32 v168, 3, v167
	v_cmp_gt_u32_e32 vcc, s23, v168
	s_nop 1
	v_cndmask_b32_e64 v18, 0, 1.0, vcc
	v_and_b32_e32 v167, 31, v8
	v_lshlrev_b32_e32 v167, 4, v167
	s_lshl_b32 s24, s12, 11
	s_add_i32 s25, s12, 7
	s_and_b32 s25, s25, 7
	s_lshl_b32 s26, s25, 11
	v_or_b32_e32 v4, s24, v167
	v_or_b32_e32 v5, s26, v167
	s_lshl_b32 s28, s25, 2
	s_add_u32 s28, s28, 0x10000
	v_mov_b32_e32 v7, s28
	v_mov_b32_e32 v19, 0
	v_mov_b32_e32 v20, 0
	v_mov_b32_e32 v21, 0
	v_mov_b32_e32 v22, 0
	s_waitcnt lgkmcnt(0)
	v_cmp_lt_u32_e64 s[32:33], 31, v8
	v_cmp_gt_u32_e64 s[34:35], 32, v8
	v_pack_b32_f16 v24, v188, v189
	v_pack_b32_f16 v25, v190, v191
	v_pack_b32_f16 v26, v192, v193
	v_pack_b32_f16 v27, v194, v195
	v_pack_b32_f16 v167, v196, v197
	v_cndmask_b32_e64 v28, 0, v167, s[32:33]
	v_cndmask_b32_e64 v32, 0, v167, s[34:35]
	v_pack_b32_f16 v167, v198, v199
	v_cndmask_b32_e64 v29, 0, v167, s[32:33]
	v_cndmask_b32_e64 v33, 0, v167, s[34:35]
	v_pack_b32_f16 v167, v200, v201
	v_cndmask_b32_e64 v30, 0, v167, s[32:33]
	v_cndmask_b32_e64 v34, 0, v167, s[34:35]
	v_pack_b32_f16 v167, v202, v203
	v_cndmask_b32_e64 v31, 0, v167, s[32:33]
	v_cndmask_b32_e64 v35, 0, v167, s[34:35]
	s_waitcnt lgkmcnt(0)
	s_barrier
	s_cmp_lt_u32 s12, 4
	s_cbranch_scc1 .Lq_noprio
	s_setprio 1
